# union12 + attention tile loop: the end-of-unit / no-QK block cluster moved out of line so the common per-tile path falls straight into the P.V block
# speedup vs baseline: 1.0033x; 1.0033x over previous
.LBB0_397:
	s_add_i32 s0, s34, 0x80
	s_cmp_le_u32 s0, s24
	s_cselect_b64 s[78:79], -1, 0
	s_add_i32 s82, s31, 0
	s_add_i32 s3, s34, 0x13f
	s_cmp_gt_u32 s3, s16
	s_cselect_b64 s[36:37], -1, 0
	s_cmp_gt_u32 s0, s24
	s_cbranch_scc1 .Latt_noqk
	v_add_u32_e32 v152, s82, v164
	v_xor_b32_e32 v220, 32, v152
	v_xor_b32_e32 v221, 64, v152
	v_xor_b32_e32 v222, 0x60, v152
	ds_read_b128 v[204:207], v152
	ds_read_b128 v[208:211], v152 offset:4096
	ds_read_b128 v[212:215], v220
	ds_read_b128 v[216:219], v220 offset:4096
	s_add_i32 s0, s73, 0
	v_add_u32_e32 v196, s0, v171
	v_add_u32_e32 v197, s0, v170
	v_add_u32_e32 v202, s0, v169
	v_add_u32_e32 v203, s0, v168
	ds_read_b64_tr_b16 v[178:179], v196 offset:16384
	ds_read_b64_tr_b16 v[180:181], v197 offset:16384
	ds_read_b64_tr_b16 v[184:185], v197 offset:20480
	ds_read_b64_tr_b16 v[182:183], v196 offset:20480
	ds_read_b64_tr_b16 v[186:187], v202 offset:16384
	ds_read_b64_tr_b16 v[188:189], v203 offset:16384
	ds_read_b64_tr_b16 v[192:193], v203 offset:20480
	ds_read_b64_tr_b16 v[190:191], v202 offset:20480
	v_cndmask_b32_e64 v68, v165, 0, s[36:37]
	v_sub_f32_e32 v68, v68, v167
	v_mov_b32_e32 v82, v68
	v_mov_b32_e32 v83, v68
	v_mov_b32_e32 v69, v68
	v_mov_b32_e32 v70, v68
	v_mov_b32_e32 v71, v68
	v_mov_b32_e32 v72, v68
	v_mov_b32_e32 v73, v68
	v_mov_b32_e32 v74, v68
	v_mov_b32_e32 v75, v68
	v_mov_b32_e32 v76, v68
	v_mov_b32_e32 v77, v68
	v_mov_b32_e32 v78, v68
	v_mov_b32_e32 v79, v68
	v_mov_b32_e32 v80, v68
	v_mov_b32_e32 v81, v68
	s_nop 1
	s_waitcnt lgkmcnt(11)
	v_mfma_f32_32x32x16_bf16 v[100:115], v[204:207], v[116:119], v[68:83]
	s_waitcnt lgkmcnt(10)
	v_mfma_f32_32x32x16_bf16 v[84:99], v[208:211], v[116:119], v[68:83]
	s_waitcnt lgkmcnt(9)
	v_mfma_f32_32x32x16_bf16 v[100:115], v[212:215], v[120:123], v[100:115]
	ds_read_b128 v[204:207], v221
	ds_read_b128 v[208:211], v221 offset:4096
	ds_read_b128 v[212:215], v222
	s_waitcnt lgkmcnt(11)
	v_mfma_f32_32x32x16_bf16 v[84:99], v[216:219], v[120:123], v[84:99]
	ds_read_b128 v[216:219], v222 offset:4096
	s_waitcnt lgkmcnt(3)
	v_mfma_f32_32x32x16_bf16 v[100:115], v[204:207], v[124:127], v[100:115]
	s_waitcnt lgkmcnt(2)
	v_mfma_f32_32x32x16_bf16 v[84:99], v[208:211], v[124:127], v[84:99]
	s_waitcnt lgkmcnt(1)
	v_mfma_f32_32x32x16_bf16 v[68:83], v[212:215], v[128:131], v[100:115]
	s_waitcnt lgkmcnt(0)
	v_mfma_f32_32x32x16_bf16 v[84:99], v[216:219], v[128:131], v[84:99]
	s_andn2_b64 vcc, exec, s[36:37]
	s_cbranch_vccz .Latt_near
.LBB0_432:
	s_add_i32 s34, s34, 64
	s_cmp_gt_u32 s34, s24
	s_cbranch_scc1 .LBB0_433

; #define WG_BAR() do { asm volatile("s_waitcnt vmcnt(0) lgkmcnt(0)" ::: "memory"); __builtin_amdgcn_s_barrier(); asm volatile("" ::: "memory"); } while (0)
; __device__ __forceinline__ float half_swap_sum(float m) { unsigned a = __builtin_bit_cast(unsigned, m), b = a; half_swap(a, b); return __builtin_bit_cast(float, a) + __builtin_bit_cast(float, b); }
; __device__ __forceinline__ void attn_unit(LAS unsigned char* lds, const bf16* proj, bf16* Y, const float* relb, const float* hgain, float lam, float oscale, int b, int h, int qb, int tid, int lane, int wid, Stopwatch& sw) {
;     ...
;     WG_BAR();
;     if (mp == 0) {
;         float ss = 0.f;
; #pragma unroll
;         for (int c = 0; c < 4; ++c)
; #pragma unroll
;             for (int r = 0; r < 16; ++r) { const float d = o[c][r] * inv - lam * xch[((wq * 64 + c * 16 + r) << 6) + lane]; o[c][r] = d; ss += d * d; }
;         ss = half_swap_sum(ss);
;         const float rs = oscale / sqrtf(ss * (1.f / 128.f) + NORM_EPS);
.LBB0_444:
	s_waitcnt vmcnt(0) lgkmcnt(0)
	s_barrier
	s_andn2_b64 vcc, exec, s[72:73]
	s_cbranch_vccnz .LBB0_343
	global_load_dwordx4 v[136:139], v2, s[74:75]
	global_load_dwordx4 v[140:143], v2, s[74:75] offset:32
	global_load_dwordx4 v[144:147], v2, s[74:75] offset:64
	global_load_dwordx4 v[152:155], v2, s[74:75] offset:96
	global_load_dwordx4 v[156:159], v2, s[74:75] offset:128
	global_load_dwordx4 v[168:171], v2, s[74:75] offset:160
	global_load_dwordx4 v[172:175], v2, s[74:75] offset:192
	global_load_dwordx4 v[176:179], v2, s[74:75] offset:224
	global_load_dwordx4 v[180:183], v2, s[74:75] offset:256
	global_load_dwordx4 v[184:187], v2, s[74:75] offset:288
	global_load_dwordx4 v[188:191], v2, s[74:75] offset:320
	global_load_dwordx4 v[192:195], v2, s[74:75] offset:352
	global_load_dwordx4 v[204:207], v2, s[74:75] offset:384
	global_load_dwordx4 v[208:211], v2, s[74:75] offset:416
	global_load_dwordx4 v[212:215], v2, s[74:75] offset:448
	global_load_dwordx4 v[216:219], v2, s[74:75] offset:480
	v_readlane_b32 s0, v253, 9
	v_readlane_b32 s24, v253, 61
	v_readlane_b32 s25, v253, 62
	v_lshl_add_u32 v76, v166, 2, s0
	ds_read2st64_b32 v[70:71], v76 offset1:1
	ds_read2st64_b32 v[68:69], v76 offset0:2 offset1:3
	ds_read2st64_b32 v[74:75], v76 offset0:4 offset1:5
	ds_read2st64_b32 v[72:73], v76 offset0:6 offset1:7
	ds_read2st64_b32 v[78:79], v76 offset0:8 offset1:9
	ds_read2st64_b32 v[82:83], v76 offset0:10 offset1:11
	s_waitcnt lgkmcnt(7)
	ds_read2st64_b32 v[126:127], v76 offset0:12 offset1:13
	s_waitcnt lgkmcnt(7)
	ds_read2st64_b32 v[128:129], v76 offset0:14 offset1:15
	ds_read2st64_b32 v[130:131], v76 offset0:16 offset1:17
	ds_read2st64_b32 v[132:133], v76 offset0:18 offset1:19
	ds_read2st64_b32 v[122:123], v76 offset0:20 offset1:21
	ds_read2st64_b32 v[124:125], v76 offset0:22 offset1:23
	ds_read2st64_b32 v[118:119], v76 offset0:24 offset1:25
	ds_read2st64_b32 v[120:121], v76 offset0:26 offset1:27
	ds_read2st64_b32 v[114:115], v76 offset0:28 offset1:29
	ds_read2st64_b32 v[116:117], v76 offset0:30 offset1:31
	ds_read2st64_b32 v[110:111], v76 offset0:32 offset1:33
	ds_read2st64_b32 v[112:113], v76 offset0:34 offset1:35
	ds_read2st64_b32 v[106:107], v76 offset0:36 offset1:37
	ds_read2st64_b32 v[108:109], v76 offset0:38 offset1:39
	ds_read2st64_b32 v[102:103], v76 offset0:40 offset1:41
	ds_read2st64_b32 v[104:105], v76 offset0:42 offset1:43
	ds_read2st64_b32 v[98:99], v76 offset0:44 offset1:45
	ds_read2st64_b32 v[100:101], v76 offset0:46 offset1:47
	ds_read2st64_b32 v[94:95], v76 offset0:48 offset1:49
	ds_read2st64_b32 v[96:97], v76 offset0:50 offset1:51
	ds_read2st64_b32 v[90:91], v76 offset0:52 offset1:53
	ds_read2st64_b32 v[92:93], v76 offset0:54 offset1:55
	ds_read2st64_b32 v[86:87], v76 offset0:56 offset1:57
	ds_read2st64_b32 v[88:89], v76 offset0:58 offset1:59
	ds_read2st64_b32 v[84:85], v76 offset0:60 offset1:61
	ds_read2st64_b32 v[76:77], v76 offset0:62 offset1:63
	s_waitcnt lgkmcnt(14)
	v_pk_mul_f32 v[68:69], v[148:149], v[68:69]
	s_lshl_b32 s34, s18, 1
	v_pk_fma_f32 v[68:69], v[54:55], v[80:81], v[68:69] op_sel_hi:[1,0,1] neg_lo:[0,0,1] neg_hi:[0,0,1]
	v_pk_mul_f32 v[54:55], v[148:149], v[70:71]
	s_waitcnt lgkmcnt(0)
	v_pk_mul_f32 v[76:77], v[148:149], v[76:77]
	v_pk_fma_f32 v[70:71], v[52:53], v[80:81], v[54:55] op_sel_hi:[1,0,1] neg_lo:[0,0,1] neg_hi:[0,0,1]
	v_pk_fma_f32 v[18:19], v[18:19], v[80:81], v[76:77] op_sel_hi:[1,0,1] neg_lo:[0,0,1] neg_hi:[0,0,1]
	v_mov_b64_e32 v[76:77], s[24:25]
	v_mad_u64_u32 v[76:77], s[24:25], v151, s67, v[76:77]
	v_mov_b32_e32 v134, v77
	v_mad_u64_u32 v[134:135], s[24:25], v163, s67, v[134:135]
	v_mul_f32_e32 v52, v71, v71
	v_mov_b32_e32 v77, v134
	v_pk_fma_f32 v[52:53], v[70:71], v[70:71], v[52:53] op_sel_hi:[1,1,0]
	v_pk_mul_f32 v[72:73], v[148:149], v[72:73]
	v_lshl_add_u64 v[76:77], v[76:77], 0, s[34:35]
	v_pk_fma_f32 v[52:53], v[68:69], v[68:69], v[52:53]
	v_mul_f32_e32 v54, v69, v69
	v_mov_b32_e32 v151, v3
	v_pk_fma_f32 v[72:73], v[58:59], v[80:81], v[72:73] op_sel_hi:[1,0,1] neg_lo:[0,0,1] neg_hi:[0,0,1]
	v_pk_mul_f32 v[58:59], v[148:149], v[74:75]
	v_pk_add_f32 v[54:55], v[52:53], v[54:55] op_sel_hi:[1,0]
	v_lshl_add_u64 v[52:53], v[76:77], 0, v[150:151]
	v_lshl_add_u64 v[52:53], v[52:53], 0, v[150:151]
	v_pk_fma_f32 v[76:77], v[56:57], v[80:81], v[58:59] op_sel_hi:[1,0,1] neg_lo:[0,0,1] neg_hi:[0,0,1]
	s_nop 0
	v_pk_fma_f32 v[54:55], v[76:77], v[76:77], v[54:55]
	v_mul_f32_e32 v56, v77, v77
	v_pk_add_f32 v[54:55], v[54:55], v[56:57] op_sel_hi:[1,0]
	v_mul_f32_e32 v56, v73, v73
	v_pk_fma_f32 v[54:55], v[72:73], v[72:73], v[54:55]
	s_nop 0
	v_pk_add_f32 v[54:55], v[54:55], v[56:57] op_sel_hi:[1,0]
	v_pk_mul_f32 v[56:57], v[148:149], v[82:83]
	s_nop 0
	v_pk_fma_f32 v[74:75], v[62:63], v[80:81], v[56:57] op_sel_hi:[1,0,1] neg_lo:[0,0,1] neg_hi:[0,0,1]
	v_pk_mul_f32 v[56:57], v[148:149], v[78:79]
	s_nop 0
	v_pk_fma_f32 v[82:83], v[60:61], v[80:81], v[56:57] op_sel_hi:[1,0,1] neg_lo:[0,0,1] neg_hi:[0,0,1]
	s_nop 0
	v_pk_fma_f32 v[54:55], v[82:83], v[82:83], v[54:55]
	v_mul_f32_e32 v56, v83, v83
	v_pk_add_f32 v[54:55], v[54:55], v[56:57] op_sel_hi:[1,0]
	v_mul_f32_e32 v56, v75, v75
	v_pk_fma_f32 v[54:55], v[74:75], v[74:75], v[54:55]
	s_nop 0
	v_pk_add_f32 v[54:55], v[54:55], v[56:57] op_sel_hi:[1,0]
	v_pk_mul_f32 v[56:57], v[148:149], v[128:129]
	s_nop 0
	v_pk_fma_f32 v[66:67], v[66:67], v[80:81], v[56:57] op_sel_hi:[1,0,1] neg_lo:[0,0,1] neg_hi:[0,0,1]
	v_pk_mul_f32 v[56:57], v[148:149], v[126:127]
	s_nop 0
	v_pk_fma_f32 v[78:79], v[64:65], v[80:81], v[56:57] op_sel_hi:[1,0,1] neg_lo:[0,0,1] neg_hi:[0,0,1]
	s_nop 0
	v_pk_fma_f32 v[54:55], v[78:79], v[78:79], v[54:55]
	v_mul_f32_e32 v56, v79, v79
; __device__ __forceinline__ float half_swap_sum(float m) { unsigned a = __builtin_bit_cast(unsigned, m), b = a; half_swap(a, b); return __builtin_bit_cast(float, a) + __builtin_bit_cast(float, b); }
; __device__ __forceinline__ void attn_unit(LAS unsigned char* lds, const bf16* proj, bf16* Y, const float* relb, const float* hgain, float lam, float oscale, int b, int h, int qb, int tid, int lane, int wid, Stopwatch& sw) {
;     ...
;     if (mp == 0) {
;         float ss = 0.f;
; #pragma unroll
;         for (int c = 0; c < 4; ++c)
; #pragma unroll
;             for (int r = 0; r < 16; ++r) { const float d = o[c][r] * inv - lam * xch[((wq * 64 + c * 16 + r) << 6) + lane]; o[c][r] = d; ss += d * d; }
;         ss = half_swap_sum(ss);
	v_pk_add_f32 v[54:55], v[54:55], v[56:57] op_sel_hi:[1,0]
	v_mul_f32_e32 v56, v67, v67
	v_pk_fma_f32 v[54:55], v[66:67], v[66:67], v[54:55]
	s_nop 0
	v_pk_add_f32 v[54:55], v[54:55], v[56:57] op_sel_hi:[1,0]
	v_pk_mul_f32 v[56:57], v[148:149], v[132:133]
	s_nop 0
	v_pk_fma_f32 v[60:61], v[38:39], v[80:81], v[56:57] op_sel_hi:[1,0,1] neg_lo:[0,0,1] neg_hi:[0,0,1]
	v_pk_mul_f32 v[38:39], v[148:149], v[130:131]
	s_nop 0
	v_pk_fma_f32 v[64:65], v[36:37], v[80:81], v[38:39] op_sel_hi:[1,0,1] neg_lo:[0,0,1] neg_hi:[0,0,1]
	s_nop 0
	v_pk_fma_f32 v[36:37], v[64:65], v[64:65], v[54:55]
	v_mul_f32_e32 v38, v65, v65
	v_pk_add_f32 v[36:37], v[36:37], v[38:39] op_sel_hi:[1,0]
	v_mul_f32_e32 v38, v61, v61
	v_pk_fma_f32 v[36:37], v[60:61], v[60:61], v[36:37]
	s_nop 0
	v_pk_add_f32 v[36:37], v[36:37], v[38:39] op_sel_hi:[1,0]
	v_pk_mul_f32 v[38:39], v[148:149], v[124:125]
	s_nop 0
	v_pk_fma_f32 v[56:57], v[42:43], v[80:81], v[38:39] op_sel_hi:[1,0,1] neg_lo:[0,0,1] neg_hi:[0,0,1]
	v_pk_mul_f32 v[38:39], v[148:149], v[122:123]
	s_nop 0
	v_pk_fma_f32 v[62:63], v[40:41], v[80:81], v[38:39] op_sel_hi:[1,0,1] neg_lo:[0,0,1] neg_hi:[0,0,1]
	s_nop 0
	v_pk_fma_f32 v[36:37], v[62:63], v[62:63], v[36:37]
	v_mul_f32_e32 v38, v63, v63
	v_pk_add_f32 v[36:37], v[36:37], v[38:39] op_sel_hi:[1,0]
	v_mul_f32_e32 v38, v57, v57
	v_pk_fma_f32 v[36:37], v[56:57], v[56:57], v[36:37]
	s_nop 0
	v_pk_add_f32 v[36:37], v[36:37], v[38:39] op_sel_hi:[1,0]
	v_pk_mul_f32 v[38:39], v[148:149], v[120:121]
	s_nop 0
	v_pk_fma_f32 v[54:55], v[46:47], v[80:81], v[38:39] op_sel_hi:[1,0,1] neg_lo:[0,0,1] neg_hi:[0,0,1]
	v_pk_mul_f32 v[38:39], v[148:149], v[118:119]
	s_nop 0
	v_pk_fma_f32 v[58:59], v[44:45], v[80:81], v[38:39] op_sel_hi:[1,0,1] neg_lo:[0,0,1] neg_hi:[0,0,1]
	s_nop 0
	v_pk_fma_f32 v[36:37], v[58:59], v[58:59], v[36:37]
	v_mul_f32_e32 v38, v59, v59
	v_pk_add_f32 v[36:37], v[36:37], v[38:39] op_sel_hi:[1,0]
	v_mul_f32_e32 v38, v55, v55
	v_pk_fma_f32 v[36:37], v[54:55], v[54:55], v[36:37]
	s_nop 0
	v_pk_add_f32 v[36:37], v[36:37], v[38:39] op_sel_hi:[1,0]
	v_pk_mul_f32 v[38:39], v[148:149], v[116:117]
	s_nop 0
	v_pk_fma_f32 v[44:45], v[50:51], v[80:81], v[38:39] op_sel_hi:[1,0,1] neg_lo:[0,0,1] neg_hi:[0,0,1]
	v_pk_mul_f32 v[38:39], v[148:149], v[114:115]
	s_nop 0
	v_pk_fma_f32 v[48:49], v[48:49], v[80:81], v[38:39] op_sel_hi:[1,0,1] neg_lo:[0,0,1] neg_hi:[0,0,1]
	s_nop 0
	v_pk_fma_f32 v[36:37], v[48:49], v[48:49], v[36:37]
	v_mul_f32_e32 v38, v49, v49
	v_pk_add_f32 v[36:37], v[36:37], v[38:39] op_sel_hi:[1,0]
	v_mul_f32_e32 v38, v45, v45
	v_pk_fma_f32 v[36:37], v[44:45], v[44:45], v[36:37]
	s_nop 0
	v_pk_add_f32 v[36:37], v[36:37], v[38:39] op_sel_hi:[1,0]
	v_pk_mul_f32 v[38:39], v[148:149], v[112:113]
	s_nop 0
	v_pk_fma_f32 v[40:41], v[22:23], v[80:81], v[38:39] op_sel_hi:[1,0,1] neg_lo:[0,0,1] neg_hi:[0,0,1]
	v_pk_mul_f32 v[22:23], v[148:149], v[110:111]
	s_nop 0
	v_pk_fma_f32 v[46:47], v[20:21], v[80:81], v[22:23] op_sel_hi:[1,0,1] neg_lo:[0,0,1] neg_hi:[0,0,1]
	s_nop 0
	v_pk_fma_f32 v[20:21], v[46:47], v[46:47], v[36:37]
	v_mul_f32_e32 v22, v47, v47
	v_pk_add_f32 v[20:21], v[20:21], v[22:23] op_sel_hi:[1,0]
	v_mul_f32_e32 v22, v41, v41
	v_pk_fma_f32 v[20:21], v[40:41], v[40:41], v[20:21]
	s_nop 0
	v_pk_add_f32 v[20:21], v[20:21], v[22:23] op_sel_hi:[1,0]
	v_pk_mul_f32 v[22:23], v[148:149], v[108:109]
	s_nop 0
	v_pk_fma_f32 v[36:37], v[26:27], v[80:81], v[22:23] op_sel_hi:[1,0,1] neg_lo:[0,0,1] neg_hi:[0,0,1]
	v_pk_mul_f32 v[22:23], v[148:149], v[106:107]
	s_nop 0
	v_pk_fma_f32 v[42:43], v[24:25], v[80:81], v[22:23] op_sel_hi:[1,0,1] neg_lo:[0,0,1] neg_hi:[0,0,1]
	s_nop 0
	v_pk_fma_f32 v[20:21], v[42:43], v[42:43], v[20:21]
	v_mul_f32_e32 v22, v43, v43
	v_pk_add_f32 v[20:21], v[20:21], v[22:23] op_sel_hi:[1,0]
	v_mul_f32_e32 v22, v37, v37
	v_pk_fma_f32 v[20:21], v[36:37], v[36:37], v[20:21]
	s_nop 0
	v_pk_add_f32 v[20:21], v[20:21], v[22:23] op_sel_hi:[1,0]
	v_pk_mul_f32 v[22:23], v[148:149], v[104:105]
	s_nop 0
	v_pk_fma_f32 v[30:31], v[30:31], v[80:81], v[22:23] op_sel_hi:[1,0,1] neg_lo:[0,0,1] neg_hi:[0,0,1]
	v_pk_mul_f32 v[22:23], v[148:149], v[102:103]
	s_nop 0
	v_pk_fma_f32 v[38:39], v[28:29], v[80:81], v[22:23] op_sel_hi:[1,0,1] neg_lo:[0,0,1] neg_hi:[0,0,1]
	s_nop 0
	v_pk_fma_f32 v[20:21], v[38:39], v[38:39], v[20:21]
	v_mul_f32_e32 v22, v39, v39
	v_pk_add_f32 v[20:21], v[20:21], v[22:23] op_sel_hi:[1,0]
	v_mul_f32_e32 v22, v31, v31
	v_pk_fma_f32 v[20:21], v[30:31], v[30:31], v[20:21]
	s_nop 0
	v_pk_add_f32 v[20:21], v[20:21], v[22:23] op_sel_hi:[1,0]
	v_pk_mul_f32 v[22:23], v[148:149], v[100:101]
	s_nop 0
	v_pk_fma_f32 v[24:25], v[34:35], v[80:81], v[22:23] op_sel_hi:[1,0,1] neg_lo:[0,0,1] neg_hi:[0,0,1]
	v_pk_mul_f32 v[22:23], v[148:149], v[98:99]
	s_nop 0
	v_pk_fma_f32 v[28:29], v[32:33], v[80:81], v[22:23] op_sel_hi:[1,0,1] neg_lo:[0,0,1] neg_hi:[0,0,1]
	s_nop 0
	v_pk_fma_f32 v[20:21], v[28:29], v[28:29], v[20:21]
	v_mul_f32_e32 v22, v29, v29
	v_pk_add_f32 v[20:21], v[20:21], v[22:23] op_sel_hi:[1,0]
	v_mul_f32_e32 v22, v25, v25
	v_pk_fma_f32 v[20:21], v[24:25], v[24:25], v[20:21]
	s_nop 0
	v_pk_add_f32 v[22:23], v[20:21], v[22:23] op_sel_hi:[1,0]
	v_pk_mul_f32 v[20:21], v[148:149], v[96:97]
	s_nop 0
	v_pk_fma_f32 v[20:21], v[6:7], v[80:81], v[20:21] op_sel_hi:[1,0,1] neg_lo:[0,0,1] neg_hi:[0,0,1]
	v_pk_mul_f32 v[6:7], v[148:149], v[94:95]
	s_nop 0
	v_pk_fma_f32 v[26:27], v[4:5], v[80:81], v[6:7] op_sel_hi:[1,0,1] neg_lo:[0,0,1] neg_hi:[0,0,1]
	s_nop 0
	v_pk_fma_f32 v[4:5], v[26:27], v[26:27], v[22:23]
	v_mul_f32_e32 v6, v27, v27
	v_pk_add_f32 v[4:5], v[4:5], v[6:7] op_sel_hi:[1,0]
	v_mul_f32_e32 v6, v21, v21
	v_pk_fma_f32 v[4:5], v[20:21], v[20:21], v[4:5]
; #define GAS __attribute__((address_space(1)))
; __device__ __forceinline__ unsigned pk2(float lo, float hi) { f32x2_t_ v = {lo, hi}; bf16x2_t_ b = __builtin_convertvector(v, bf16x2_t_); return __builtin_bit_cast(unsigned, b); }
; __device__ __forceinline__ float half_swap_sum(float m) { unsigned a = __builtin_bit_cast(unsigned, m), b = a; half_swap(a, b); return __builtin_bit_cast(float, a) + __builtin_bit_cast(float, b); }
; __device__ __forceinline__ void attn_unit(LAS unsigned char* lds, const bf16* proj, bf16* Y, const float* relb, const float* hgain, float lam, float oscale, int b, int h, int qb, int tid, int lane, int wid, Stopwatch& sw) {
;     ...
;         ss = half_swap_sum(ss);
;         const float rs = oscale / sqrtf(ss * (1.f / 128.f) + NORM_EPS);
;         bf16* yp = Y + (rowbase + qi) * LDY + 1024 + h * 128;
; #pragma unroll
;         for (int c = 0; c < 4; ++c)
; #pragma unroll
;             for (int r4 = 0; r4 < 4; ++r4) { const int dv = 32 * c + 8 * r4 + 4 * hi; const f32x4 g = *(const GAS f32x4*)(hgain + dv);
;                 v2u w; w.x = pk2(o[c][4 * r4] * rs * g.x, o[c][4 * r4 + 1] * rs * g.y); w.y = pk2(o[c][4 * r4 + 2] * rs * g.z, o[c][4 * r4 + 3] * rs * g.w);
	s_nop 0
	v_pk_add_f32 v[4:5], v[4:5], v[6:7] op_sel_hi:[1,0]
	v_pk_mul_f32 v[6:7], v[148:149], v[92:93]
	s_nop 0
	v_pk_fma_f32 v[10:11], v[10:11], v[80:81], v[6:7] op_sel_hi:[1,0,1] neg_lo:[0,0,1] neg_hi:[0,0,1]
	v_pk_mul_f32 v[6:7], v[148:149], v[90:91]
	s_nop 0
	v_pk_fma_f32 v[22:23], v[8:9], v[80:81], v[6:7] op_sel_hi:[1,0,1] neg_lo:[0,0,1] neg_hi:[0,0,1]
	v_pk_mul_f32 v[8:9], v[148:149], v[86:87]
	v_pk_fma_f32 v[4:5], v[22:23], v[22:23], v[4:5]
	v_mul_f32_e32 v6, v23, v23
	v_pk_add_f32 v[4:5], v[4:5], v[6:7] op_sel_hi:[1,0]
	v_mul_f32_e32 v6, v11, v11
	v_pk_fma_f32 v[4:5], v[10:11], v[10:11], v[4:5]
	v_pk_fma_f32 v[8:9], v[12:13], v[80:81], v[8:9] op_sel_hi:[1,0,1] neg_lo:[0,0,1] neg_hi:[0,0,1]
	v_pk_add_f32 v[6:7], v[4:5], v[6:7] op_sel_hi:[1,0]
	v_pk_mul_f32 v[4:5], v[148:149], v[88:89]
	v_pk_fma_f32 v[6:7], v[8:9], v[8:9], v[6:7]
	v_mul_f32_e32 v12, v9, v9
	v_pk_fma_f32 v[4:5], v[14:15], v[80:81], v[4:5] op_sel_hi:[1,0,1] neg_lo:[0,0,1] neg_hi:[0,0,1]
	v_pk_add_f32 v[6:7], v[6:7], v[12:13] op_sel_hi:[1,0]
	v_mul_f32_e32 v12, v5, v5
	v_pk_fma_f32 v[6:7], v[4:5], v[4:5], v[6:7]
	s_nop 0
	v_pk_add_f32 v[12:13], v[6:7], v[12:13] op_sel_hi:[1,0]
	v_pk_mul_f32 v[6:7], v[148:149], v[84:85]
	s_nop 0
	v_pk_fma_f32 v[6:7], v[16:17], v[80:81], v[6:7] op_sel_hi:[1,0,1] neg_lo:[0,0,1] neg_hi:[0,0,1]
	s_nop 0
	v_pk_fma_f32 v[12:13], v[6:7], v[6:7], v[12:13]
	v_mul_f32_e32 v14, v7, v7
	v_pk_add_f32 v[12:13], v[12:13], v[14:15] op_sel_hi:[1,0]
	v_mul_f32_e32 v14, v19, v19
	v_pk_fma_f32 v[12:13], v[18:19], v[18:19], v[12:13]
	s_nop 0
	v_pk_add_f32 v[12:13], v[12:13], v[14:15] op_sel_hi:[1,0]
	s_nop 0
	v_mov_b32_e32 v13, v12
	s_nop 1
	v_permlane32_swap_b32 v12, v13
	s_nop 1
	s_nop 0
	v_add_f32_e32 v12, v12, v13
	v_fmamk_f32 v12, v12, 0x3c000000, v240
	v_cmp_gt_f32_e32 vcc, s82, v12
	v_mul_f32_e32 v13, 0x4f800000, v12
	s_nop 0
	v_cndmask_b32_e32 v12, v12, v13, vcc
	v_sqrt_f32_e32 v13, v12
	s_nop 0
	v_add_u32_e32 v14, -1, v13
	v_fma_f32 v15, -v14, v13, v12
	v_cmp_ge_f32_e64 s[36:37], 0, v15
	v_add_u32_e32 v15, 1, v13
	s_nop 0
	v_cndmask_b32_e64 v14, v13, v14, s[36:37]
	v_fma_f32 v13, -v15, v13, v12
	v_cmp_lt_f32_e64 s[36:37], 0, v13
	s_nop 1
	v_cndmask_b32_e64 v13, v14, v15, s[36:37]
	v_mul_f32_e32 v14, 0x37800000, v13
	v_cndmask_b32_e32 v13, v13, v14, vcc
	v_cmp_class_f32_e32 vcc, v12, v241
	s_nop 1
	v_cndmask_b32_e32 v12, v13, v12, vcc
	v_div_scale_f32 v13, s[18:19], v12, v12, v162
	v_rcp_f32_e32 v14, v13
	s_nop 0
	v_fma_f32 v15, -v13, v14, 1.0
	v_fmac_f32_e32 v14, v15, v14
	v_div_scale_f32 v15, vcc, v162, v12, v162
	v_mul_f32_e32 v16, v15, v14
	v_fma_f32 v17, -v13, v16, v15
	v_fmac_f32_e32 v16, v17, v14
	v_fma_f32 v13, -v13, v16, v15
	v_div_fmas_f32 v13, v13, v14, v16
	v_div_fixup_f32 v12, v13, v12, v162
	v_pk_mul_f32 v[32:33], v[70:71], v[12:13] op_sel_hi:[1,0]
	v_pk_mul_f32 v[30:31], v[30:31], v[12:13] op_sel_hi:[1,0]
	v_pk_mul_f32 v[28:29], v[28:29], v[12:13] op_sel_hi:[1,0]
	v_pk_mul_f32 v[24:25], v[24:25], v[12:13] op_sel_hi:[1,0]
	v_pk_mul_f32 v[20:21], v[20:21], v[12:13] op_sel_hi:[1,0]
	v_pk_mul_f32 v[10:11], v[10:11], v[12:13] op_sel_hi:[1,0]
	v_pk_mul_f32 v[8:9], v[8:9], v[12:13] op_sel_hi:[1,0]
	v_pk_mul_f32 v[4:5], v[4:5], v[12:13] op_sel_hi:[1,0]
	s_waitcnt vmcnt(0)
; #define GAS __attribute__((address_space(1)))
; __device__ __forceinline__ unsigned pk2(float lo, float hi) { f32x2_t_ v = {lo, hi}; bf16x2_t_ b = __builtin_convertvector(v, bf16x2_t_); return __builtin_bit_cast(unsigned, b); }
; __device__ __forceinline__ void attn_unit(LAS unsigned char* lds, const bf16* proj, bf16* Y, const float* relb, const float* hgain, float lam, float oscale, int b, int h, int qb, int tid, int lane, int wid, Stopwatch& sw) {
;     ...
; #pragma unroll
;         for (int c = 0; c < 4; ++c)
; #pragma unroll
;             for (int r4 = 0; r4 < 4; ++r4) { const int dv = 32 * c + 8 * r4 + 4 * hi; const f32x4 g = *(const GAS f32x4*)(hgain + dv);
;                 v2u w; w.x = pk2(o[c][4 * r4] * rs * g.x, o[c][4 * r4 + 1] * rs * g.y); w.y = pk2(o[c][4 * r4 + 2] * rs * g.z, o[c][4 * r4 + 3] * rs * g.w);
;                 *(GAS v2u*)(yp + dv) = w; }
	v_pk_mul_f32 v[14:15], v[136:137], v[32:33]
	v_pk_mul_f32 v[32:33], v[68:69], v[12:13] op_sel_hi:[1,0]
	v_cvt_pk_bf16_f32 v220, v14, v15
	v_pk_mul_f32 v[16:17], v[138:139], v[32:33]
	v_pk_mul_f32 v[32:33], v[76:77], v[12:13] op_sel_hi:[1,0]
	v_cvt_pk_bf16_f32 v221, v16, v17
	v_pk_mul_f32 v[14:15], v[140:141], v[32:33]
	v_pk_mul_f32 v[32:33], v[72:73], v[12:13] op_sel_hi:[1,0]
	v_cvt_pk_bf16_f32 v222, v14, v15
	v_pk_mul_f32 v[16:17], v[142:143], v[32:33]
	v_pk_mul_f32 v[32:33], v[82:83], v[12:13] op_sel_hi:[1,0]
	v_cvt_pk_bf16_f32 v223, v16, v17
	s_nop 1
	v_permlane32_swap_b32 v220, v222
	v_permlane32_swap_b32 v221, v223
	global_store_dwordx4 v[52:53], v[220:223], off offset:2048
	v_pk_mul_f32 v[14:15], v[144:145], v[32:33]
	v_pk_mul_f32 v[32:33], v[74:75], v[12:13] op_sel_hi:[1,0]
	v_cvt_pk_bf16_f32 v224, v14, v15
	v_pk_mul_f32 v[16:17], v[146:147], v[32:33]
	v_pk_mul_f32 v[32:33], v[78:79], v[12:13] op_sel_hi:[1,0]
	v_cvt_pk_bf16_f32 v225, v16, v17
	v_pk_mul_f32 v[14:15], v[152:153], v[32:33]
	v_pk_mul_f32 v[32:33], v[66:67], v[12:13] op_sel_hi:[1,0]
	v_cvt_pk_bf16_f32 v226, v14, v15
	v_pk_mul_f32 v[16:17], v[154:155], v[32:33]
	v_pk_mul_f32 v[32:33], v[64:65], v[12:13] op_sel_hi:[1,0]
	v_cvt_pk_bf16_f32 v227, v16, v17
	s_nop 1
	v_permlane32_swap_b32 v224, v226
	v_permlane32_swap_b32 v225, v227
	global_store_dwordx4 v[52:53], v[224:227], off offset:2080
	v_pk_mul_f32 v[14:15], v[32:33], v[156:157]
	v_pk_mul_f32 v[32:33], v[60:61], v[12:13] op_sel_hi:[1,0]
	v_cvt_pk_bf16_f32 v220, v14, v15
	v_pk_mul_f32 v[16:17], v[32:33], v[158:159]
	v_pk_mul_f32 v[32:33], v[62:63], v[12:13] op_sel_hi:[1,0]
	v_cvt_pk_bf16_f32 v221, v16, v17
	v_pk_mul_f32 v[14:15], v[32:33], v[168:169]
	v_pk_mul_f32 v[32:33], v[56:57], v[12:13] op_sel_hi:[1,0]
	v_cvt_pk_bf16_f32 v222, v14, v15
	v_pk_mul_f32 v[16:17], v[32:33], v[170:171]
	v_pk_mul_f32 v[32:33], v[58:59], v[12:13] op_sel_hi:[1,0]
	v_cvt_pk_bf16_f32 v223, v16, v17
	s_nop 1
	v_permlane32_swap_b32 v220, v222
	v_permlane32_swap_b32 v221, v223
	global_store_dwordx4 v[52:53], v[220:223], off offset:2112
	v_pk_mul_f32 v[14:15], v[32:33], v[172:173]
	v_pk_mul_f32 v[32:33], v[54:55], v[12:13] op_sel_hi:[1,0]
	v_cvt_pk_bf16_f32 v224, v14, v15
	v_pk_mul_f32 v[16:17], v[32:33], v[174:175]
	v_pk_mul_f32 v[32:33], v[48:49], v[12:13] op_sel_hi:[1,0]
	v_cvt_pk_bf16_f32 v225, v16, v17
	v_pk_mul_f32 v[14:15], v[32:33], v[176:177]
	v_pk_mul_f32 v[32:33], v[44:45], v[12:13] op_sel_hi:[1,0]
	v_cvt_pk_bf16_f32 v226, v14, v15
	v_pk_mul_f32 v[16:17], v[32:33], v[178:179]
	v_pk_mul_f32 v[32:33], v[46:47], v[12:13] op_sel_hi:[1,0]
	v_cvt_pk_bf16_f32 v227, v16, v17
	s_nop 1
	v_permlane32_swap_b32 v224, v226
	v_permlane32_swap_b32 v225, v227
	global_store_dwordx4 v[52:53], v[224:227], off offset:2144
	v_pk_mul_f32 v[14:15], v[32:33], v[180:181]
	v_pk_mul_f32 v[32:33], v[40:41], v[12:13] op_sel_hi:[1,0]
	v_cvt_pk_bf16_f32 v220, v14, v15
	v_pk_mul_f32 v[16:17], v[32:33], v[182:183]
	v_pk_mul_f32 v[32:33], v[42:43], v[12:13] op_sel_hi:[1,0]
	v_cvt_pk_bf16_f32 v221, v16, v17
	v_pk_mul_f32 v[14:15], v[32:33], v[184:185]
	v_pk_mul_f32 v[32:33], v[36:37], v[12:13] op_sel_hi:[1,0]
	v_cvt_pk_bf16_f32 v222, v14, v15
	v_pk_mul_f32 v[16:17], v[32:33], v[186:187]
	v_pk_mul_f32 v[32:33], v[38:39], v[12:13] op_sel_hi:[1,0]
	v_cvt_pk_bf16_f32 v223, v16, v17
	s_nop 1
	v_permlane32_swap_b32 v220, v222
	v_permlane32_swap_b32 v221, v223
	global_store_dwordx4 v[52:53], v[220:223], off offset:2176
	v_pk_mul_f32 v[14:15], v[32:33], v[188:189]
	v_pk_mul_f32 v[16:17], v[30:31], v[190:191]
	v_cvt_pk_bf16_f32 v224, v14, v15
	v_cvt_pk_bf16_f32 v225, v16, v17
	v_pk_mul_f32 v[14:15], v[28:29], v[192:193]
	v_pk_mul_f32 v[16:17], v[24:25], v[194:195]
	v_cvt_pk_bf16_f32 v226, v14, v15
	v_cvt_pk_bf16_f32 v227, v16, v17
	s_nop 1
	v_permlane32_swap_b32 v224, v226
	v_permlane32_swap_b32 v225, v227
	global_store_dwordx4 v[52:53], v[224:227], off offset:2208
	v_pk_mul_f32 v[24:25], v[26:27], v[12:13] op_sel_hi:[1,0]
	v_pk_mul_f32 v[16:17], v[20:21], v[206:207]
	v_pk_mul_f32 v[14:15], v[24:25], v[204:205]
	v_pk_mul_f32 v[20:21], v[22:23], v[12:13] op_sel_hi:[1,0]
	v_cvt_pk_bf16_f32 v220, v14, v15
	v_cvt_pk_bf16_f32 v221, v16, v17
	v_pk_mul_f32 v[14:15], v[20:21], v[208:209]
	v_pk_mul_f32 v[10:11], v[10:11], v[210:211]
	v_cvt_pk_bf16_f32 v222, v14, v15
	v_cvt_pk_bf16_f32 v223, v10, v11
	s_nop 1
	v_permlane32_swap_b32 v220, v222
	v_permlane32_swap_b32 v221, v223
	global_store_dwordx4 v[52:53], v[220:223], off offset:2240
	v_pk_mul_f32 v[8:9], v[8:9], v[212:213]
	v_pk_mul_f32 v[4:5], v[4:5], v[214:215]
	v_cvt_pk_bf16_f32 v224, v8, v9
	v_cvt_pk_bf16_f32 v225, v4, v5
	v_pk_mul_f32 v[4:5], v[6:7], v[12:13] op_sel_hi:[1,0]
	v_pk_mul_f32 v[6:7], v[18:19], v[12:13] op_sel_hi:[1,0]
	v_pk_mul_f32 v[4:5], v[4:5], v[216:217]
	v_pk_mul_f32 v[6:7], v[6:7], v[218:219]
	v_cvt_pk_bf16_f32 v226, v4, v5
	v_cvt_pk_bf16_f32 v227, v6, v7
	s_nop 1
	v_permlane32_swap_b32 v224, v226
	v_permlane32_swap_b32 v225, v227
	global_store_dwordx4 v[52:53], v[224:227], off offset:2272
	s_branch .LBB0_343
.LBB0_433:
	s_andn2_b64 vcc, exec, s[78:79]
	s_cbranch_vccz .LBB0_436
	s_branch .LBB0_439

.LBB0_434:
	s_add_i32 s34, s34, 64
	s_cmp_gt_u32 s34, s24
	s_cbranch_scc1 .LBB0_433
	s_branch .LBB0_435
